# baseline (speedup 1.0000x reference)
.LBB2_22:
	s_and_b64 vcc, exec, s[4:5]
	s_cbranch_vccz .LBB2_275
	s_load_dwordx2 s[8:9], s[0:1], 0x10
	s_load_dwordx2 s[98:99], s[0:1], 0x0
	v_lshlrev_b32_e32 v100, 2, v0
	s_mul_i32 s100, s2, 0x6000
	v_add_u32_e32 v101, 0x1000, v100
	v_add_u32_e32 v102, 0x2000, v100
	v_add_u32_e32 v103, 0x3000, v100
	v_add_u32_e32 v104, 0x4000, v100
	v_add_u32_e32 v105, 0x5000, v100
	s_waitcnt lgkmcnt(0)
	s_add_u32 s98, s98, s100
	s_addc_u32 s99, s99, 0
	global_load_dword v76, v100, s[98:99]
	global_load_dword v77, v100, s[98:99] offset:1024
	global_load_dword v78, v100, s[98:99] offset:2048
	global_load_dword v79, v100, s[98:99] offset:3072
	global_load_dword v80, v101, s[98:99]
	global_load_dword v81, v101, s[98:99] offset:1024
	global_load_dword v82, v101, s[98:99] offset:2048
	global_load_dword v83, v101, s[98:99] offset:3072
	global_load_dword v84, v102, s[98:99]
	global_load_dword v85, v102, s[98:99] offset:1024
	global_load_dword v86, v102, s[98:99] offset:2048
	global_load_dword v87, v102, s[98:99] offset:3072
	global_load_dword v88, v103, s[98:99]
	global_load_dword v89, v103, s[98:99] offset:1024
	global_load_dword v90, v103, s[98:99] offset:2048
	global_load_dword v91, v103, s[98:99] offset:3072
	global_load_dword v92, v104, s[98:99]
	global_load_dword v93, v104, s[98:99] offset:1024
	global_load_dword v94, v104, s[98:99] offset:2048
	global_load_dword v95, v104, s[98:99] offset:3072
	global_load_dword v96, v105, s[98:99]
	global_load_dword v97, v105, s[98:99] offset:1024
	global_load_dword v98, v105, s[98:99] offset:2048
	global_load_dword v99, v105, s[98:99] offset:3072
	s_movk_i32 s3, 0xc4
	v_cmp_gt_u32_e32 vcc, s3, v0
	v_mov_b32_e32 v4, 0
	v_mov_b32_e32 v1, 0
	s_and_saveexec_b64 s[4:5], vcc
	s_cbranch_execz .LBB2_25
	v_lshlrev_b32_e32 v1, 8, v0
	s_waitcnt lgkmcnt(0)
	global_load_dword v1, v1, s[8:9]

.LBB2_47:
	s_mul_i32 s4, s2, 0x6000
	s_add_u32 s66, s10, s4
	s_addc_u32 s67, s11, 0
	v_cmp_gt_i32_e64 s[48:49], s3, v0
	s_and_saveexec_b64 s[4:5], s[48:49]
	s_cbranch_execz .LBB2_49
	v_mov_b32_e32 v1, v76
.LBB2_49:
	s_or_b64 exec, exec, s[4:5]
	s_min_i32 s33, s3, 0x1800
	v_or_b32_e32 v3, 0x100, v0
	v_cmp_gt_i32_e64 s[46:47], s33, v3
	v_mov_b32_e32 v38, 0
	v_mov_b32_e32 v50, 0
	s_and_saveexec_b64 s[4:5], s[46:47]
	s_cbranch_execz .LBB2_51
	v_mov_b32_e32 v50, v77
.LBB2_51:
	s_or_b64 exec, exec, s[4:5]
	v_or_b32_e32 v3, 0x200, v0
	v_cmp_gt_i32_e64 s[44:45], s33, v3
	s_and_saveexec_b64 s[4:5], s[44:45]
	s_cbranch_execz .LBB2_53
	v_mov_b32_e32 v38, v78
.LBB2_53:
	s_or_b64 exec, exec, s[4:5]
	v_or_b32_e32 v3, 0x300, v0
	v_cmp_gt_i32_e64 s[42:43], s33, v3
	v_mov_b32_e32 v37, 0
	v_mov_b32_e32 v49, 0
	s_and_saveexec_b64 s[4:5], s[42:43]
	s_cbranch_execz .LBB2_55
	v_mov_b32_e32 v49, v79
.LBB2_55:
	s_or_b64 exec, exec, s[4:5]
	v_or_b32_e32 v28, 0x400, v0
	v_cmp_gt_i32_e64 s[40:41], s33, v28
	s_and_saveexec_b64 s[4:5], s[40:41]
	s_cbranch_execz .LBB2_57
	v_lshlrev_b32_e32 v3, 2, v28
	v_mov_b32_e32 v37, v80
.LBB2_57:
	s_or_b64 exec, exec, s[4:5]
	v_or_b32_e32 v27, 0x500, v0
	v_cmp_gt_i32_e64 s[38:39], s33, v27
	v_mov_b32_e32 v36, 0
	v_mov_b32_e32 v48, 0
	s_and_saveexec_b64 s[4:5], s[38:39]
	s_cbranch_execz .LBB2_59
	v_lshlrev_b32_e32 v3, 2, v27
	v_mov_b32_e32 v48, v81
.LBB2_59:
	s_or_b64 exec, exec, s[4:5]
	v_or_b32_e32 v26, 0x600, v0
	v_cmp_gt_i32_e64 s[36:37], s33, v26
	s_and_saveexec_b64 s[4:5], s[36:37]
	s_cbranch_execz .LBB2_61
	v_lshlrev_b32_e32 v3, 2, v26
	v_mov_b32_e32 v36, v82
.LBB2_61:
	s_or_b64 exec, exec, s[4:5]
	v_or_b32_e32 v25, 0x700, v0
	v_cmp_gt_i32_e64 s[34:35], s33, v25
	v_mov_b32_e32 v35, 0
	v_mov_b32_e32 v47, 0
	s_and_saveexec_b64 s[4:5], s[34:35]
	s_cbranch_execz .LBB2_63
	v_lshlrev_b32_e32 v3, 2, v25
	v_mov_b32_e32 v47, v83
.LBB2_63:
	s_or_b64 exec, exec, s[4:5]
	v_or_b32_e32 v24, 0x800, v0
	v_cmp_gt_i32_e64 s[30:31], s33, v24
	s_and_saveexec_b64 s[4:5], s[30:31]
	s_cbranch_execz .LBB2_65
	v_lshlrev_b32_e32 v3, 2, v24
	v_mov_b32_e32 v35, v84
.LBB2_65:
	s_or_b64 exec, exec, s[4:5]
	v_or_b32_e32 v23, 0x900, v0
	v_cmp_gt_i32_e64 s[28:29], s33, v23
	v_mov_b32_e32 v34, 0
	v_mov_b32_e32 v46, 0
	s_and_saveexec_b64 s[4:5], s[28:29]
	s_cbranch_execz .LBB2_67
	v_lshlrev_b32_e32 v3, 2, v23
	v_mov_b32_e32 v46, v85
.LBB2_67:
	s_or_b64 exec, exec, s[4:5]
	v_or_b32_e32 v22, 0xa00, v0
	v_cmp_gt_i32_e64 s[26:27], s33, v22
	s_and_saveexec_b64 s[4:5], s[26:27]
	s_cbranch_execz .LBB2_69
	v_lshlrev_b32_e32 v3, 2, v22
	v_mov_b32_e32 v34, v86
.LBB2_69:
	s_or_b64 exec, exec, s[4:5]
	v_or_b32_e32 v21, 0xb00, v0
	v_cmp_gt_i32_e64 s[24:25], s33, v21
	v_mov_b32_e32 v33, 0
	v_mov_b32_e32 v45, 0
	s_and_saveexec_b64 s[4:5], s[24:25]
	s_cbranch_execz .LBB2_71
	v_lshlrev_b32_e32 v3, 2, v21
	v_mov_b32_e32 v45, v87
.LBB2_71:
	s_or_b64 exec, exec, s[4:5]
	v_or_b32_e32 v20, 0xc00, v0
	v_cmp_gt_i32_e64 s[22:23], s33, v20
	s_and_saveexec_b64 s[4:5], s[22:23]
	s_cbranch_execz .LBB2_73
	v_lshlrev_b32_e32 v3, 2, v20
	v_mov_b32_e32 v33, v88
.LBB2_73:
	s_or_b64 exec, exec, s[4:5]
	v_or_b32_e32 v19, 0xd00, v0
	v_cmp_gt_i32_e64 s[20:21], s33, v19
	v_mov_b32_e32 v32, 0
	v_mov_b32_e32 v44, 0
	s_and_saveexec_b64 s[4:5], s[20:21]
	s_cbranch_execz .LBB2_75
	v_lshlrev_b32_e32 v3, 2, v19
	v_mov_b32_e32 v44, v89
.LBB2_75:
	s_or_b64 exec, exec, s[4:5]
	v_or_b32_e32 v18, 0xe00, v0
	v_cmp_gt_i32_e64 s[18:19], s33, v18
	s_and_saveexec_b64 s[4:5], s[18:19]
	s_cbranch_execz .LBB2_77
	v_lshlrev_b32_e32 v3, 2, v18
	v_mov_b32_e32 v32, v90
.LBB2_77:
	s_or_b64 exec, exec, s[4:5]
	v_or_b32_e32 v17, 0xf00, v0
	v_cmp_gt_i32_e64 s[16:17], s33, v17
	v_mov_b32_e32 v31, 0
	v_mov_b32_e32 v43, 0
	s_and_saveexec_b64 s[4:5], s[16:17]
	s_cbranch_execz .LBB2_79
	v_lshlrev_b32_e32 v3, 2, v17
	v_mov_b32_e32 v43, v91
.LBB2_79:
	s_or_b64 exec, exec, s[4:5]
	v_or_b32_e32 v16, 0x1000, v0
	v_cmp_gt_i32_e64 s[14:15], s33, v16
	s_and_saveexec_b64 s[4:5], s[14:15]
	s_cbranch_execz .LBB2_81
	v_lshlrev_b32_e32 v3, 2, v16
	v_mov_b32_e32 v31, v92
.LBB2_81:
	s_or_b64 exec, exec, s[4:5]
	v_or_b32_e32 v15, 0x1100, v0
	v_cmp_gt_i32_e64 s[12:13], s33, v15
	v_mov_b32_e32 v30, 0
	v_mov_b32_e32 v42, 0
	s_and_saveexec_b64 s[4:5], s[12:13]
	s_cbranch_execz .LBB2_83
	v_lshlrev_b32_e32 v3, 2, v15
	v_mov_b32_e32 v42, v93
.LBB2_83:
	s_or_b64 exec, exec, s[4:5]
	v_or_b32_e32 v14, 0x1200, v0
	v_cmp_gt_i32_e64 s[10:11], s33, v14
	s_and_saveexec_b64 s[4:5], s[10:11]
	s_cbranch_execz .LBB2_85
	v_lshlrev_b32_e32 v3, 2, v14
	v_mov_b32_e32 v30, v94
.LBB2_85:
	s_or_b64 exec, exec, s[4:5]
	v_or_b32_e32 v13, 0x1300, v0
	v_cmp_gt_i32_e64 s[8:9], s33, v13
	v_mov_b32_e32 v29, 0
	v_mov_b32_e32 v41, 0
	s_and_saveexec_b64 s[4:5], s[8:9]
	s_cbranch_execz .LBB2_87
	v_lshlrev_b32_e32 v3, 2, v13
	v_mov_b32_e32 v41, v95
.LBB2_87:
	s_or_b64 exec, exec, s[4:5]
	v_or_b32_e32 v12, 0x1400, v0
	v_cmp_gt_i32_e64 s[6:7], s33, v12
	s_and_saveexec_b64 s[4:5], s[6:7]
	s_cbranch_execz .LBB2_89
	v_lshlrev_b32_e32 v3, 2, v12
	v_mov_b32_e32 v29, v96
.LBB2_89:
	s_or_b64 exec, exec, s[4:5]
	v_or_b32_e32 v11, 0x1500, v0
	v_cmp_gt_i32_e64 s[4:5], s33, v11
	v_mov_b32_e32 v3, 0
	v_mov_b32_e32 v40, 0
	s_and_saveexec_b64 s[50:51], s[4:5]
	s_cbranch_execz .LBB2_91
	v_lshlrev_b32_e32 v4, 2, v11
	v_mov_b32_e32 v40, v97
.LBB2_91:
	s_or_b64 exec, exec, s[50:51]
	v_or_b32_e32 v10, 0x1600, v0
	v_cmp_gt_i32_e64 s[68:69], s33, v10
	s_and_saveexec_b64 s[50:51], s[68:69]
	s_cbranch_execz .LBB2_93
	v_lshlrev_b32_e32 v3, 2, v10
	v_mov_b32_e32 v3, v98

.LBB2_172:
	v_lshlrev_b32_e32 v4, 2, v9
	v_mov_b32_e32 v39, v99
	s_or_b64 exec, exec, s[70:71]
	s_and_saveexec_b64 s[66:67], s[48:49]
	s_cbranch_execz .LBB2_95

	.amdhsa_kernel _Z12k_fine_gemm1PKjPKyPKiPiS5_S5_S5_PKfPK6__halfS7_S7_PS8_PfSC_
		.amdhsa_group_segment_fixed_size 53248
		.amdhsa_private_segment_fixed_size 0
		.amdhsa_kernarg_size 112
		.amdhsa_user_sgpr_count 2
		.amdhsa_user_sgpr_dispatch_ptr 0
		.amdhsa_user_sgpr_queue_ptr 0
		.amdhsa_user_sgpr_kernarg_segment_ptr 1
		.amdhsa_user_sgpr_dispatch_id 0
		.amdhsa_user_sgpr_kernarg_preload_length 0
		.amdhsa_user_sgpr_kernarg_preload_offset 0
		.amdhsa_user_sgpr_private_segment_size 0
		.amdhsa_uses_dynamic_stack 0
		.amdhsa_enable_private_segment 0
		.amdhsa_system_sgpr_workgroup_id_x 1
		.amdhsa_system_sgpr_workgroup_id_y 0
		.amdhsa_system_sgpr_workgroup_id_z 0
		.amdhsa_system_sgpr_workgroup_info 0
		.amdhsa_system_vgpr_workitem_id 0
		.amdhsa_next_free_vgpr 144
		.amdhsa_next_free_sgpr 102
		.amdhsa_accum_offset 144
		.amdhsa_reserve_vcc 1
		.amdhsa_float_round_mode_32 0
		.amdhsa_float_round_mode_16_64 0
		.amdhsa_float_denorm_mode_32 3
		.amdhsa_float_denorm_mode_16_64 3
		.amdhsa_dx10_clamp 1
		.amdhsa_ieee_mode 1
		.amdhsa_fp16_overflow 0
		.amdhsa_tg_split 0
		.amdhsa_exception_fp_ieee_invalid_op 0
		.amdhsa_exception_fp_denorm_src 0
		.amdhsa_exception_fp_ieee_div_zero 0
		.amdhsa_exception_fp_ieee_overflow 0
		.amdhsa_exception_fp_ieee_underflow 0
		.amdhsa_exception_fp_ieee_inexact 0
		.amdhsa_exception_int_div_zero 0
	.end_amdhsa_kernel

amdhsa.kernels:
  - .agpr_count:     0
    .args:
      - .actual_access:  read_only
        .address_space:  global
        .offset:         0
        .size:           8
        .value_kind:     global_buffer
      - .actual_access:  read_only
        .address_space:  global
        .offset:         8
        .size:           8
        .value_kind:     global_buffer
      - .actual_access:  write_only
        .address_space:  global
        .offset:         16
        .size:           8
        .value_kind:     global_buffer
      - .actual_access:  write_only
        .address_space:  global
        .offset:         24
        .size:           8
        .value_kind:     global_buffer
      - .actual_access:  write_only
        .address_space:  global
        .offset:         32
        .size:           8
        .value_kind:     global_buffer
    .group_segment_fixed_size: 0
    .kernarg_segment_align: 8
    .kernarg_segment_size: 40
    .language:       OpenCL C
    .language_version:
      - 2
      - 0
    .max_flat_workgroup_size: 256
    .name:           _Z6k_prepPKfS0_P6__halfS2_Pi
    .private_segment_fixed_size: 0
    .sgpr_count:     18
    .sgpr_spill_count: 0
    .symbol:         _Z6k_prepPKfS0_P6__halfS2_Pi.kd
    .uniform_work_group_size: 1
    .uses_dynamic_stack: false
    .vgpr_count:     6
    .vgpr_spill_count: 0
    .wavefront_size: 64
  - .agpr_count:     0
    .args:
      - .actual_access:  read_only
        .address_space:  global
        .offset:         0
        .size:           8
        .value_kind:     global_buffer
      - .actual_access:  read_only
        .address_space:  global
        .offset:         8
        .size:           8
        .value_kind:     global_buffer
      - .address_space:  global
        .offset:         16
        .size:           8
        .value_kind:     global_buffer
      - .actual_access:  write_only
        .address_space:  global
        .offset:         24
        .size:           8
        .value_kind:     global_buffer
      - .actual_access:  write_only
        .address_space:  global
        .offset:         32
        .size:           8
        .value_kind:     global_buffer
      - .actual_access:  read_only
        .address_space:  global
        .offset:         40
        .size:           8
        .value_kind:     global_buffer
      - .actual_access:  read_only
        .address_space:  global
        .offset:         48
        .size:           8
        .value_kind:     global_buffer
      - .actual_access:  read_only
        .address_space:  global
        .offset:         56
        .size:           8
        .value_kind:     global_buffer
      - .actual_access:  read_only
        .address_space:  global
        .offset:         64
        .size:           8
        .value_kind:     global_buffer
      - .actual_access:  write_only
        .address_space:  global
        .offset:         72
        .size:           8
        .value_kind:     global_buffer
      - .actual_access:  read_only
        .address_space:  global
        .offset:         80
        .size:           8
        .value_kind:     global_buffer
      - .actual_access:  write_only
        .address_space:  global
        .offset:         88
        .size:           8
        .value_kind:     global_buffer
    .group_segment_fixed_size: 53248
    .kernarg_segment_align: 8
    .kernarg_segment_size: 96
    .language:       OpenCL C
    .language_version:
      - 2
      - 0
    .max_flat_workgroup_size: 256
    .name:           _Z15k_scatter_gemm1PKiS0_PiPjPyPKfPK6__halfS5_S5_PS6_PfSA_
    .private_segment_fixed_size: 0
    .sgpr_count:     32
    .sgpr_spill_count: 0
    .symbol:         _Z15k_scatter_gemm1PKiS0_PiPjPyPKfPK6__halfS5_S5_PS6_PfSA_.kd
    .uniform_work_group_size: 1
    .uses_dynamic_stack: false
    .vgpr_count:     146
    .vgpr_spill_count: 0
    .wavefront_size: 64
  - .agpr_count:     0
    .args:
      - .actual_access:  read_only
        .address_space:  global
        .offset:         0
        .size:           8
        .value_kind:     global_buffer
      - .actual_access:  read_only
        .address_space:  global
        .offset:         8
        .size:           8
        .value_kind:     global_buffer
      - .actual_access:  read_only
        .address_space:  global
        .offset:         16
        .size:           8
        .value_kind:     global_buffer
      - .actual_access:  write_only
        .address_space:  global
        .offset:         24
        .size:           8
        .value_kind:     global_buffer
      - .actual_access:  write_only
        .address_space:  global
        .offset:         32
        .size:           8
        .value_kind:     global_buffer
      - .actual_access:  write_only
        .address_space:  global
        .offset:         40
        .size:           8
        .value_kind:     global_buffer
      - .actual_access:  write_only
        .address_space:  global
        .offset:         48
        .size:           8
        .value_kind:     global_buffer
      - .actual_access:  read_only
        .address_space:  global
        .offset:         56
        .size:           8
        .value_kind:     global_buffer
      - .actual_access:  read_only
        .address_space:  global
        .offset:         64
        .size:           8
        .value_kind:     global_buffer
      - .actual_access:  read_only
        .address_space:  global
        .offset:         72
        .size:           8
        .value_kind:     global_buffer
      - .actual_access:  read_only
        .address_space:  global
        .offset:         80
        .size:           8
        .value_kind:     global_buffer
      - .actual_access:  write_only
        .address_space:  global
        .offset:         88
        .size:           8
        .value_kind:     global_buffer
      - .actual_access:  read_only
        .address_space:  global
        .offset:         96
        .size:           8
        .value_kind:     global_buffer
      - .actual_access:  write_only
        .address_space:  global
        .offset:         104
        .size:           8
        .value_kind:     global_buffer
    .group_segment_fixed_size: 53248
    .kernarg_segment_align: 8
    .kernarg_segment_size: 112
    .language:       OpenCL C
    .language_version:
      - 2
      - 0
    .max_flat_workgroup_size: 256
    .name:           _Z12k_fine_gemm1PKjPKyPKiPiS5_S5_S5_PKfPK6__halfS7_S7_PS8_PfSC_
    .private_segment_fixed_size: 0
    .sgpr_count:     108
    .sgpr_spill_count: 0
    .symbol:         _Z12k_fine_gemm1PKjPKyPKiPiS5_S5_S5_PKfPK6__halfS7_S7_PS8_PfSC_.kd
    .uniform_work_group_size: 1
    .uses_dynamic_stack: false
    .vgpr_count:     144
    .vgpr_spill_count: 0
    .wavefront_size: 64
  - .agpr_count:     0
    .args:
      - .actual_access:  read_only
        .address_space:  global
        .offset:         0
        .size:           8
        .value_kind:     global_buffer
      - .actual_access:  read_only
        .address_space:  global
        .offset:         8
        .size:           8
        .value_kind:     global_buffer
      - .actual_access:  read_only
        .address_space:  global
        .offset:         16
        .size:           8
        .value_kind:     global_buffer
      - .actual_access:  read_only
        .address_space:  global
        .offset:         24
        .size:           8
        .value_kind:     global_buffer
      - .actual_access:  read_only
        .address_space:  global
        .offset:         32
        .size:           8
        .value_kind:     global_buffer
      - .actual_access:  read_only
        .address_space:  global
        .offset:         40
        .size:           8
        .value_kind:     global_buffer
      - .actual_access:  read_only
        .address_space:  global
        .offset:         48
        .size:           8
        .value_kind:     global_buffer
      - .actual_access:  read_only
        .address_space:  global
        .offset:         56
        .size:           8
        .value_kind:     global_buffer
      - .actual_access:  read_only
        .address_space:  global
        .offset:         64
        .size:           8
        .value_kind:     global_buffer
      - .actual_access:  write_only
        .address_space:  global
        .offset:         72
        .size:           8
        .value_kind:     global_buffer
      - .actual_access:  read_only
        .address_space:  global
        .offset:         80
        .size:           8
        .value_kind:     global_buffer
      - .actual_access:  write_only
        .address_space:  global
        .offset:         88
        .size:           8
        .value_kind:     global_buffer
      - .actual_access:  read_only
        .address_space:  global
        .offset:         96
        .size:           8
        .value_kind:     global_buffer
      - .actual_access:  read_only
        .address_space:  global
        .offset:         104
        .size:           8
        .value_kind:     global_buffer
      - .actual_access:  read_only
        .address_space:  global
        .offset:         112
        .size:           8
        .value_kind:     global_buffer
    .group_segment_fixed_size: 5376
    .kernarg_segment_align: 8
    .kernarg_segment_size: 120
    .language:       OpenCL C
    .language_version:
      - 2
      - 0
    .max_flat_workgroup_size: 256
    .name:           _Z6k_agg1PKiS0_PK6__halfPKfS5_S5_S3_S5_S5_PS1_PfS7_S5_S0_S0_
    .private_segment_fixed_size: 0
    .sgpr_count:     43
    .sgpr_spill_count: 0
    .symbol:         _Z6k_agg1PKiS0_PK6__halfPKfS5_S5_S3_S5_S5_PS1_PfS7_S5_S0_S0_.kd
    .uniform_work_group_size: 1
    .uses_dynamic_stack: false
    .vgpr_count:     77
    .vgpr_spill_count: 0
    .wavefront_size: 64
  - .agpr_count:     0
    .args:
      - .actual_access:  read_only
        .address_space:  global
        .offset:         0
        .size:           8
        .value_kind:     global_buffer
      - .actual_access:  read_only
        .address_space:  global
        .offset:         8
        .size:           8
        .value_kind:     global_buffer
      - .actual_access:  read_only
        .address_space:  global
        .offset:         16
        .size:           8
        .value_kind:     global_buffer
      - .actual_access:  read_only
        .address_space:  global
        .offset:         24
        .size:           8
        .value_kind:     global_buffer
      - .actual_access:  read_only
        .address_space:  global
        .offset:         32
        .size:           8
        .value_kind:     global_buffer
      - .actual_access:  read_only
        .address_space:  global
        .offset:         40
        .size:           8
        .value_kind:     global_buffer
      - .actual_access:  write_only
        .address_space:  global
        .offset:         48
        .size:           8
        .value_kind:     global_buffer
      - .actual_access:  read_only
        .address_space:  global
        .offset:         56
        .size:           8
        .value_kind:     global_buffer
      - .actual_access:  read_only
        .address_space:  global
        .offset:         64
        .size:           8
        .value_kind:     global_buffer
      - .actual_access:  read_only
        .address_space:  global
        .offset:         72
        .size:           8
        .value_kind:     global_buffer
    .group_segment_fixed_size: 1024
    .kernarg_segment_align: 8
    .kernarg_segment_size: 80
    .language:       OpenCL C
    .language_version:
      - 2
      - 0
    .max_flat_workgroup_size: 256
    .name:           _Z6k_agg2PKiS0_PK6__halfPKfS5_S5_PfS5_S0_S0_
    .private_segment_fixed_size: 0
    .sgpr_count:     28
    .sgpr_spill_count: 0
    .symbol:         _Z6k_agg2PKiS0_PK6__halfPKfS5_S5_PfS5_S0_S0_.kd
    .uniform_work_group_size: 1
    .uses_dynamic_stack: false
    .vgpr_count:     60
    .vgpr_spill_count: 0
    .wavefront_size: 64
